# combine phase: final-norm weights preloaded once before the token loop (8 per-token reloads with vmcnt(0) removed), s_nop after 16-byte stores for the store-data hazard
# speedup vs baseline: 1.0134x; 1.0062x over previous
.LBB0_2657:
	s_cmp_gt_i32 s94, 15
	s_cselect_b64 s[2:3], -1, 0
	s_xor_b64 s[0:1], s[0:1], -1
	s_or_b64 s[0:1], s[2:3], s[0:1]
	s_and_b64 vcc, exec, s[0:1]
	v_readlane_b32 s0, v237, 29
	v_readlane_b32 s8, v237, 37
	v_readlane_b32 s9, v237, 38
	v_readlane_b32 s10, v237, 39
	v_readlane_b32 s11, v237, 40
	v_readlane_b32 s12, v237, 41
	v_readlane_b32 s13, v237, 42
	v_readlane_b32 s1, v237, 30
	v_readlane_b32 s2, v237, 31
	v_readlane_b32 s3, v237, 32
	v_readlane_b32 s4, v237, 33
	v_readlane_b32 s5, v237, 34
	v_readlane_b32 s6, v237, 35
	v_readlane_b32 s7, v237, 36
	v_readlane_b32 s14, v237, 43
	v_readlane_b32 s15, v237, 44
	s_cbranch_vccnz .LBB0_2663
	v_mov_b32_e32 v1, 0x4000
	global_load_dword v1, v1, s[12:13] offset:512 sc1
	s_cmpk_gt_i32 s96, 0x3fff
	s_cbranch_scc1 .LBB0_2663
	v_readlane_b32 s12, v238, 13
	v_readlane_b32 s18, v238, 19
	v_readlane_b32 s19, v238, 20
	v_lshlrev_b32_e32 v2, 3, v0
	v_readlane_b32 s14, v238, 15
	s_mov_b64 s[6:7], s[18:19]
	v_and_b32_e32 v3, 0x1f8, v2
	v_readlane_b32 s15, v238, 16
	s_add_u32 s14, s6, 8
	v_lshlrev_b32_e32 v2, 2, v3
	v_lshlrev_b32_e32 v16, 1, v3
	v_mov_b32_e32 v17, 0
	s_addc_u32 s15, s7, 0
	s_ashr_i32 s97, s96, 31
	s_ashr_i32 s93, s92, 31
	v_lshl_add_u64 v[18:19], s[76:77], 0, v[16:17]
	v_or_b32_e32 v16, 0x1000, v2
	s_lshl_b64 s[2:3], s[96:97], 4
	s_lshl_b64 s[4:5], s[92:93], 4
	s_lshl_b64 s[0:1], s[96:97], 13
	v_lshl_add_u64 v[22:23], s[8:9], 0, v[16:17]
	v_or_b32_e32 v16, 0x1800, v2
	v_and_b32_e32 v0, 63, v0
	s_add_u32 s0, s10, s0
	v_mov_b32_e32 v3, v17
	v_lshl_add_u64 v[24:25], s[8:9], 0, v[16:17]
	v_lshlrev_b32_e32 v16, 5, v0
	s_addc_u32 s1, s11, s1
	v_lshl_add_u64 v[20:21], s[8:9], 0, v[2:3]
	v_lshl_add_u64 v[2:3], s[0:1], 0, v[16:17]
	s_mov_b64 s[0:1], 0x1000
	v_lshl_add_u64 v[26:27], v[2:3], 0, s[0:1]
	s_lshl_b64 s[6:7], s[92:93], 13
	s_lshl_b64 s[0:1], s[96:97], 12
	s_add_u32 s0, s58, s0
	v_lshlrev_b32_e32 v16, 4, v0
	s_addc_u32 s1, s59, s1
	s_waitcnt vmcnt(0)
	v_cmp_eq_u32_e32 vcc, 0, v1
	v_lshl_add_u64 v[2:3], s[0:1], 0, v[16:17]
	s_mov_b64 s[0:1], 0x800
	v_cndmask_b32_e64 v0, 0, 1, vcc
	v_lshl_add_u64 v[28:29], v[2:3], 0, s[0:1]
	s_lshl_b64 s[8:9], s[92:93], 12
	v_cmp_ne_u32_e64 s[0:1], 1, v0
	v_mov_b32_e32 v16, 0x358637bd
	v_readlane_b32 s13, v238, 14
	v_readlane_b32 s16, v238, 17
	v_readlane_b32 s17, v238, 18
	v_readlane_b32 s20, v238, 21
	v_readlane_b32 s21, v238, 22
	v_readlane_b32 s22, v238, 23
	v_readlane_b32 s23, v238, 24
	v_readlane_b32 s24, v238, 25
	v_readlane_b32 s25, v238, 26
	v_readlane_b32 s26, v238, 27
	v_readlane_b32 s27, v238, 28
	global_load_dwordx4 v[150:153], v[20:21], off
	global_load_dwordx4 v[154:157], v[20:21], off offset:16
	global_load_dwordx4 v[158:161], v[20:21], off offset:2048
	global_load_dwordx4 v[162:165], v[20:21], off offset:2064
	global_load_dwordx4 v[166:169], v[22:23], off
	global_load_dwordx4 v[170:173], v[22:23], off offset:16
	global_load_dwordx4 v[174:177], v[24:25], off
	global_load_dwordx4 v[178:181], v[24:25], off offset:16
	s_branch .LBB0_2661
.LBB0_2660:
	v_pk_mul_f32 v[44:45], v[44:45], v[4:5] op_sel_hi:[1,0]
	v_pk_mul_f32 v[52:53], v[46:47], v[4:5] op_sel_hi:[1,0]
	v_pk_mul_f32 v[36:37], v[36:37], v[4:5] op_sel_hi:[1,0]
	v_pk_mul_f32 v[14:15], v[14:15], v[4:5] op_sel_hi:[1,0]
	v_pk_mul_f32 v[32:33], v[32:33], v[4:5] op_sel_hi:[1,0]
	v_pk_mul_f32 v[6:7], v[6:7], v[4:5] op_sel_hi:[1,0]
	v_pk_mul_f32 v[12:13], v[12:13], v[4:5] op_sel_hi:[1,0]
	v_pk_mul_f32 v[10:11], v[10:11], v[4:5] op_sel_hi:[1,0]
	s_add_i32 s96, s96, s92
	v_pk_mul_f32 v[0:1], v[0:1], v[4:5] op_sel_hi:[1,0]
	s_add_u32 s2, s2, s4
	s_addc_u32 s3, s3, s5
	s_cmpk_lt_i32 s96, 0x4000
	v_lshl_add_u64 v[28:29], v[28:29], 0, s[8:9]
	v_pk_mul_f32 v[46:47], v[152:153], v[44:45]
	v_pk_mul_f32 v[44:45], v[150:151], v[52:53]
	global_store_dwordx4 v[26:27], v[44:47], off offset:-4096
	s_nop 1
	v_pk_mul_f32 v[48:49], v[38:39], v[4:5] op_sel_hi:[1,0]
	v_pk_mul_f32 v[38:39], v[36:37], v[156:157]
	v_pk_mul_f32 v[36:37], v[48:49], v[154:155]
	global_store_dwordx4 v[26:27], v[36:39], off offset:-4080
	s_nop 1
	v_pk_mul_f32 v[38:39], v[14:15], v[160:161]
	v_pk_mul_f32 v[36:37], v[32:33], v[158:159]
	global_store_dwordx4 v[26:27], v[36:39], off offset:-2048
	s_nop 1
	v_pk_mul_f32 v[32:33], v[42:43], v[4:5] op_sel_hi:[1,0]
	v_pk_mul_f32 v[14:15], v[6:7], v[164:165]
	v_pk_mul_f32 v[12:13], v[12:13], v[162:163]
	global_store_dwordx4 v[26:27], v[12:15], off offset:-2032
	s_nop 1
	v_pk_mul_f32 v[6:7], v[40:41], v[4:5] op_sel_hi:[1,0]
	v_pk_mul_f32 v[12:13], v[32:33], v[166:167]
	v_pk_mul_f32 v[14:15], v[6:7], v[168:169]
	global_store_dwordx4 v[26:27], v[12:15], off
	s_nop 1
	v_pk_mul_f32 v[6:7], v[30:31], v[4:5] op_sel_hi:[1,0]
	v_pk_mul_f32 v[30:31], v[34:35], v[4:5] op_sel_hi:[1,0]
	v_pk_mul_f32 v[14:15], v[6:7], v[172:173]
	v_pk_mul_f32 v[12:13], v[30:31], v[170:171]
	global_store_dwordx4 v[26:27], v[12:15], off offset:16
	s_nop 1
	v_pk_mul_f32 v[6:7], v[8:9], v[4:5] op_sel_hi:[1,0]
	v_pk_mul_f32 v[4:5], v[2:3], v[4:5] op_sel_hi:[1,0]
	v_pk_mul_f32 v[8:9], v[6:7], v[176:177]
	v_pk_mul_f32 v[6:7], v[10:11], v[174:175]
	global_store_dwordx4 v[26:27], v[6:9], off offset:2048
	s_nop 1
	v_pk_mul_f32 v[2:3], v[0:1], v[180:181]
	v_pk_mul_f32 v[0:1], v[4:5], v[178:179]
	global_store_dwordx4 v[26:27], v[0:3], off offset:2064
	s_nop 1
	v_lshl_add_u64 v[26:27], v[26:27], 0, s[6:7]
	s_cbranch_scc0 .LBB0_2663
